# P6 epilogue x loads nt (on top of P1 + conversion nt stores)
# baseline (speedup 1.0000x reference)
.LBB0_847:
	v_lshl_add_u32 v130, s38, 8, v1
	v_ashrrev_i32_e32 v131, 31, v130
	s_lshl_b32 s40, s34, 8
	v_lshlrev_b64 v[130:131], 10, v[130:131]
	s_ashr_i32 s41, s40, 31
	v_lshl_add_u64 v[226:227], v[130:131], 0, s[40:41]
	v_or_b32_e32 v226, v226, v202
	v_lshl_add_u64 v[178:179], v[226:227], 2, s[36:37]
	global_load_dwordx4 v[208:211], v[178:179], off nt
	global_load_dwordx4 v[212:215], v[178:179], off offset:16 nt
	s_mov_b64 s[40:41], 0x10000
	v_add_co_u32_e32 v180, vcc, s61, v178
	v_lshl_add_u64 v[130:131], v[178:179], 0, s[40:41]
	s_nop 0
	v_addc_co_u32_e32 v181, vcc, 0, v179, vcc
	s_mov_b32 s23, 0x20000
	global_load_dwordx4 v[216:219], v[180:181], off nt
	global_load_dwordx4 v[222:225], v[130:131], off offset:16 nt
	v_add_co_u32_e32 v182, vcc, s23, v178
	s_mov_b64 s[40:41], 0x20000
	s_nop 0
	v_addc_co_u32_e32 v183, vcc, 0, v179, vcc
	global_load_dwordx4 v[162:165], v[182:183], off nt
	v_lshl_add_u64 v[130:131], v[178:179], 0, s[40:41]
	s_mov_b32 s23, 0x30000
	global_load_dwordx4 v[150:153], v[130:131], off offset:16 nt
	v_add_co_u32_e32 v184, vcc, s23, v178
	s_mov_b64 s[42:43], 0x30000
	s_nop 0
	v_addc_co_u32_e32 v185, vcc, 0, v179, vcc
	s_mov_b32 s25, 0x80000
	v_lshl_add_u64 v[130:131], v[178:179], 0, s[42:43]
	global_load_dwordx4 v[166:169], v[184:185], off nt
	global_load_dwordx4 v[154:157], v[130:131], off offset:16 nt
	s_mov_b64 s[40:41], 0x80000
	v_add_co_u32_e32 v186, vcc, s25, v178
	v_lshl_add_u64 v[130:131], v[178:179], 0, s[40:41]
	s_nop 0
	v_addc_co_u32_e32 v187, vcc, 0, v179, vcc
	s_mov_b32 s23, 0x90000
	global_load_dwordx4 v[174:177], v[186:187], off nt
	global_load_dwordx4 v[170:173], v[130:131], off offset:16 nt
	v_add_co_u32_e32 v192, vcc, s23, v178
	s_mov_b64 s[42:43], 0x90000
	s_nop 0
	v_addc_co_u32_e32 v193, vcc, 0, v179, vcc
	s_mov_b32 s34, 0xa0000
	v_lshl_add_u64 v[130:131], v[178:179], 0, s[42:43]
	global_load_dwordx4 v[158:161], v[192:193], off nt
	global_load_dwordx4 v[146:149], v[130:131], off offset:16 nt
	v_add_co_u32_e32 v190, vcc, s34, v178
	s_mov_b64 s[44:45], 0xa0000
	s_mov_b32 s25, 0xb0000
	v_addc_co_u32_e32 v191, vcc, 0, v179, vcc
	v_lshl_add_u64 v[132:133], v[178:179], 0, s[44:45]
	v_add_co_u32_e32 v188, vcc, s25, v178
	global_load_dwordx4 v[142:145], v[190:191], off nt
	global_load_dwordx4 v[138:141], v[132:133], off offset:16 nt
	s_mov_b64 s[40:41], 0xb0000
	v_addc_co_u32_e32 v189, vcc, 0, v179, vcc
	v_lshl_add_u64 v[228:229], v[178:179], 0, s[40:41]
	global_load_dwordx4 v[134:137], v[188:189], off nt
	global_load_dwordx4 v[130:133], v[228:229], off offset:16 nt
	s_mov_b32 s23, 0x58000
	s_waitcnt vmcnt(0)
	v_pk_add_f32 v[228:229], v[128:129], v[210:211]
	v_pk_add_f32 v[230:231], v[126:127], v[208:209]
	v_pk_add_f32 v[232:233], v[124:125], v[214:215]
	v_pk_add_f32 v[214:215], v[122:123], v[212:213]
	v_lshlrev_b64 v[208:209], 1, v[226:227]
	v_lshl_add_u64 v[210:211], s[2:3], 0, v[208:209]
	v_cvt_pk_bf16_f32 v212, v230, v231
	v_cvt_pk_bf16_f32 v213, v228, v229
	v_cvt_pk_bf16_f32 v214, v214, v215
	v_cvt_pk_bf16_f32 v215, v232, v233
	global_store_dwordx4 v[210:211], v[212:215], off
	v_or_b32_e32 v208, 0x100, v208
	v_pk_add_f32 v[162:163], v[110:111], v[162:163]
	v_pk_add_f32 v[214:215], v[120:121], v[218:219]
	v_pk_add_f32 v[212:213], v[118:119], v[216:217]
	v_pk_add_f32 v[216:217], v[116:117], v[224:225]
	v_pk_add_f32 v[218:219], v[114:115], v[222:223]
	v_cvt_pk_bf16_f32 v212, v212, v213
	v_cvt_pk_bf16_f32 v213, v214, v215
	v_cvt_pk_bf16_f32 v215, v216, v217
	v_add_co_u32_e32 v216, vcc, s65, v210
	v_cvt_pk_bf16_f32 v214, v218, v219
	s_nop 0
	v_addc_co_u32_e32 v217, vcc, 0, v211, vcc
	global_store_dwordx4 v[216:217], v[212:215], off
	v_pk_add_f32 v[164:165], v[112:113], v[164:165]
	v_pk_add_f32 v[154:155], v[98:99], v[154:155]
	v_pk_add_f32 v[212:213], v[108:109], v[152:153]
	v_pk_add_f32 v[152:153], v[106:107], v[150:151]
	v_cvt_pk_bf16_f32 v150, v162, v163
	v_add_co_u32_e32 v162, vcc, s61, v210
	v_cvt_pk_bf16_f32 v151, v164, v165
	v_cvt_pk_bf16_f32 v152, v152, v153
	v_cvt_pk_bf16_f32 v153, v212, v213
	v_addc_co_u32_e32 v163, vcc, 0, v211, vcc
	global_store_dwordx4 v[162:163], v[150:153], off
	v_pk_add_f32 v[156:157], v[100:101], v[156:157]
	v_pk_add_f32 v[142:143], v[46:47], v[142:143]
	v_pk_add_f32 v[152:153], v[104:105], v[168:169]
	v_pk_add_f32 v[150:151], v[102:103], v[166:167]
	v_pk_add_f32 v[144:145], v[48:49], v[144:145]
	v_cvt_pk_bf16_f32 v150, v150, v151
	v_cvt_pk_bf16_f32 v151, v152, v153
	v_cvt_pk_bf16_f32 v152, v154, v155
	v_add_co_u32_e32 v154, vcc, s64, v210
	v_cvt_pk_bf16_f32 v153, v156, v157
	s_nop 0
	v_addc_co_u32_e32 v155, vcc, 0, v211, vcc
	global_store_dwordx4 v[154:155], v[150:153], off
	v_pk_add_f32 v[154:155], v[60:61], v[172:173]
	v_pk_add_f32 v[156:157], v[58:59], v[170:171]
	v_pk_add_f32 v[152:153], v[64:65], v[176:177]
	v_pk_add_f32 v[150:151], v[62:63], v[174:175]
	v_pk_add_f32 v[134:135], v[38:39], v[134:135]
	v_cvt_pk_bf16_f32 v150, v150, v151
	v_cvt_pk_bf16_f32 v151, v152, v153
	v_cvt_pk_bf16_f32 v153, v154, v155
	v_add_co_u32_e32 v154, vcc, s66, v210
	v_cvt_pk_bf16_f32 v152, v156, v157
	s_nop 0
	v_addc_co_u32_e32 v155, vcc, 0, v211, vcc
	global_store_dwordx4 v[154:155], v[150:153], off
	v_pk_add_f32 v[154:155], v[52:53], v[148:149]
	v_pk_add_f32 v[148:149], v[50:51], v[146:147]
	v_pk_add_f32 v[150:151], v[56:57], v[160:161]
	v_pk_add_f32 v[152:153], v[54:55], v[158:159]
	v_cvt_pk_bf16_f32 v147, v150, v151
	v_add_co_u32_e32 v150, vcc, s67, v210
	v_cvt_pk_bf16_f32 v146, v152, v153
	v_cvt_pk_bf16_f32 v148, v148, v149
	v_cvt_pk_bf16_f32 v149, v154, v155
	v_addc_co_u32_e32 v151, vcc, 0, v211, vcc
	global_store_dwordx4 v[150:151], v[146:149], off
	v_pk_add_f32 v[136:137], v[40:41], v[136:137]
	v_lshl_add_u64 v[150:151], v[178:179], 0, s[10:11]
	v_pk_add_f32 v[146:147], v[44:45], v[140:141]
	v_pk_add_f32 v[140:141], v[42:43], v[138:139]
	v_cvt_pk_bf16_f32 v138, v142, v143
	v_add_co_u32_e32 v142, vcc, s68, v210
	v_cvt_pk_bf16_f32 v139, v144, v145
	v_cvt_pk_bf16_f32 v140, v140, v141
	v_cvt_pk_bf16_f32 v141, v146, v147
	v_addc_co_u32_e32 v143, vcc, 0, v211, vcc
	global_store_dwordx4 v[142:143], v[138:141], off
	v_lshl_add_u64 v[142:143], v[178:179], 0, s[8:9]
	v_lshl_add_u64 v[158:159], v[178:179], 0, s[12:13]
	v_pk_add_f32 v[138:139], v[36:37], v[132:133]
	v_pk_add_f32 v[132:133], v[34:35], v[130:131]
	v_cvt_pk_bf16_f32 v130, v134, v135
	v_add_co_u32_e32 v134, vcc, s23, v210
	v_cvt_pk_bf16_f32 v131, v136, v137
	v_cvt_pk_bf16_f32 v132, v132, v133
	v_cvt_pk_bf16_f32 v133, v138, v139
	v_addc_co_u32_e32 v135, vcc, 0, v211, vcc
	global_store_dwordx4 v[134:135], v[130:133], off
	global_load_dwordx4 v[130:133], v[178:179], off offset:512 nt
	s_nop 0
	global_load_dwordx4 v[134:137], v[178:179], off offset:528 nt
	global_load_dwordx4 v[138:141], v[180:181], off offset:512 nt
	s_nop 0
	global_load_dwordx4 v[142:145], v[142:143], off offset:16 nt
	s_nop 0
	global_load_dwordx4 v[146:149], v[182:183], off offset:512 nt
	s_nop 0
	global_load_dwordx4 v[150:153], v[150:151], off offset:16 nt
	s_nop 0
	global_load_dwordx4 v[154:157], v[184:185], off offset:512 nt
	s_nop 0
	global_load_dwordx4 v[158:161], v[158:159], off offset:16 nt
	s_nop 0
	global_load_dwordx4 v[162:165], v[186:187], off offset:512 nt
	v_lshl_add_u64 v[166:167], v[178:179], 0, s[14:15]
	global_load_dwordx4 v[166:169], v[166:167], off offset:16 nt
	s_nop 0
	global_load_dwordx4 v[170:173], v[192:193], off offset:512 nt
	v_lshl_add_u64 v[174:175], v[178:179], 0, s[16:17]
	global_load_dwordx4 v[174:177], v[174:175], off offset:16 nt
	v_lshl_add_u64 v[192:193], v[178:179], 0, s[18:19]
	global_load_dwordx4 v[180:183], v[190:191], off offset:512 nt
	v_lshl_add_u64 v[178:179], v[178:179], 0, s[20:21]
	global_load_dwordx4 v[184:187], v[188:189], off offset:512 nt
	s_nop 0
	global_load_dwordx4 v[188:191], v[192:193], off offset:16 nt
	global_load_dwordx4 v[210:213], v[178:179], off offset:16 nt
	v_lshl_add_u64 v[178:179], s[2:3], 0, v[208:209]
	s_waitcnt vmcnt(15)
	v_pk_add_f32 v[132:133], v[96:97], v[132:133]
	v_pk_add_f32 v[130:131], v[94:95], v[130:131]
	s_waitcnt vmcnt(14)
	v_pk_add_f32 v[136:137], v[92:93], v[136:137]
	v_pk_add_f32 v[134:135], v[90:91], v[134:135]
	v_cvt_pk_bf16_f32 v130, v130, v131
	v_cvt_pk_bf16_f32 v131, v132, v133
	v_cvt_pk_bf16_f32 v132, v134, v135
	v_cvt_pk_bf16_f32 v133, v136, v137
	global_store_dwordx4 v[178:179], v[130:133], off
	s_waitcnt vmcnt(13)
	v_pk_add_f32 v[134:135], v[84:85], v[144:145]
	v_pk_add_f32 v[136:137], v[82:83], v[142:143]
	v_pk_add_f32 v[132:133], v[88:89], v[140:141]
	v_pk_add_f32 v[130:131], v[86:87], v[138:139]
	s_nop 0
	v_cvt_pk_bf16_f32 v130, v130, v131
	v_cvt_pk_bf16_f32 v131, v132, v133
	v_cvt_pk_bf16_f32 v133, v134, v135
	v_add_co_u32_e32 v134, vcc, s65, v178
	v_cvt_pk_bf16_f32 v132, v136, v137
	s_nop 0
	v_addc_co_u32_e32 v135, vcc, 0, v179, vcc
	global_store_dwordx4 v[134:135], v[130:133], off
	s_waitcnt vmcnt(12)
	v_pk_add_f32 v[134:135], v[76:77], v[152:153]
	v_pk_add_f32 v[136:137], v[74:75], v[150:151]
	v_pk_add_f32 v[132:133], v[80:81], v[148:149]
	v_pk_add_f32 v[130:131], v[78:79], v[146:147]
	s_nop 0
	v_cvt_pk_bf16_f32 v130, v130, v131
	v_cvt_pk_bf16_f32 v131, v132, v133
	v_cvt_pk_bf16_f32 v133, v134, v135
	v_add_co_u32_e32 v134, vcc, s61, v178
	v_cvt_pk_bf16_f32 v132, v136, v137
	s_nop 0
	v_addc_co_u32_e32 v135, vcc, 0, v179, vcc
	global_store_dwordx4 v[134:135], v[130:133], off
	s_waitcnt vmcnt(11)
	v_pk_add_f32 v[134:135], v[68:69], v[160:161]
	v_pk_add_f32 v[136:137], v[66:67], v[158:159]
	v_pk_add_f32 v[132:133], v[72:73], v[156:157]
	v_pk_add_f32 v[130:131], v[70:71], v[154:155]
	s_nop 0
	v_cvt_pk_bf16_f32 v130, v130, v131
	v_cvt_pk_bf16_f32 v131, v132, v133
	v_cvt_pk_bf16_f32 v133, v134, v135
	v_add_co_u32_e32 v134, vcc, s64, v178
	v_cvt_pk_bf16_f32 v132, v136, v137
	s_nop 0
	v_addc_co_u32_e32 v135, vcc, 0, v179, vcc
	global_store_dwordx4 v[134:135], v[130:133], off
	s_waitcnt vmcnt(10)
	v_pk_add_f32 v[134:135], v[28:29], v[168:169]
	v_pk_add_f32 v[136:137], v[26:27], v[166:167]
	v_pk_add_f32 v[132:133], v[32:33], v[164:165]
	v_pk_add_f32 v[130:131], v[30:31], v[162:163]
	s_nop 0
	v_cvt_pk_bf16_f32 v130, v130, v131
	v_cvt_pk_bf16_f32 v131, v132, v133
	v_cvt_pk_bf16_f32 v133, v134, v135
	v_add_co_u32_e32 v134, vcc, s66, v178
	v_cvt_pk_bf16_f32 v132, v136, v137
	s_nop 0
	v_addc_co_u32_e32 v135, vcc, 0, v179, vcc
	global_store_dwordx4 v[134:135], v[130:133], off
	s_waitcnt vmcnt(9)
	v_pk_add_f32 v[134:135], v[20:21], v[176:177]
	v_pk_add_f32 v[136:137], v[18:19], v[174:175]
	v_pk_add_f32 v[132:133], v[24:25], v[172:173]
	v_pk_add_f32 v[130:131], v[22:23], v[170:171]
	s_nop 0
	v_cvt_pk_bf16_f32 v130, v130, v131
	v_cvt_pk_bf16_f32 v131, v132, v133
	v_cvt_pk_bf16_f32 v133, v134, v135
	v_add_co_u32_e32 v134, vcc, s67, v178
	v_cvt_pk_bf16_f32 v132, v136, v137
	s_nop 0
	v_addc_co_u32_e32 v135, vcc, 0, v179, vcc
	global_store_dwordx4 v[134:135], v[130:133], off
	s_waitcnt vmcnt(7)
	v_pk_add_f32 v[134:135], v[12:13], v[190:191]
	v_pk_add_f32 v[136:137], v[10:11], v[188:189]
	v_pk_add_f32 v[132:133], v[16:17], v[182:183]
	v_pk_add_f32 v[130:131], v[14:15], v[180:181]
	s_nop 0
	v_cvt_pk_bf16_f32 v130, v130, v131
	v_cvt_pk_bf16_f32 v131, v132, v133
	v_cvt_pk_bf16_f32 v133, v134, v135
	v_add_co_u32_e32 v134, vcc, s68, v178
	v_cvt_pk_bf16_f32 v132, v136, v137
	s_nop 0
	v_addc_co_u32_e32 v135, vcc, 0, v179, vcc
	global_store_dwordx4 v[134:135], v[130:133], off
	s_waitcnt vmcnt(7)
	v_pk_add_f32 v[134:135], v[4:5], v[212:213]
	v_pk_add_f32 v[136:137], v[2:3], v[210:211]
	v_pk_add_f32 v[132:133], v[8:9], v[186:187]
	v_pk_add_f32 v[130:131], v[6:7], v[184:185]
	s_nop 0
	v_cvt_pk_bf16_f32 v130, v130, v131
	v_cvt_pk_bf16_f32 v131, v132, v133
	v_cvt_pk_bf16_f32 v133, v134, v135
	v_add_co_u32_e32 v134, vcc, 0x58000, v178
	v_cvt_pk_bf16_f32 v132, v136, v137
	s_nop 0
	v_addc_co_u32_e32 v135, vcc, 0, v179, vcc
	s_andn2_b64 vcc, exec, s[28:29]
	s_mov_b64 s[28:29], -1
	global_store_dwordx4 v[134:135], v[130:133], off
	s_cbranch_vccnz .LBB0_832
	s_andn2_b64 vcc, exec, s[0:1]
	s_cbranch_vccnz .LBB0_831
	s_barrier
	s_branch .LBB0_831
